# baseline (speedup 1.0000x reference)
.LBB2_31:
	v_add_f32_e32 v188, v188, v192
	v_exp_f32_e32 v49, v40
	v_add_f32_e32 v40, v80, v81
	v_add_f32_e32 v40, v40, v82
	v_add_f32_e32 v40, v40, v83
	v_add_f32_e32 v40, v40, v84
	v_exp_f32_e32 v62, v41
	v_exp_f32_e32 v63, v42
	v_exp_f32_e32 v64, v43
	v_exp_f32_e32 v65, v44
	v_exp_f32_e32 v66, v45
	v_exp_f32_e32 v67, v46
	v_exp_f32_e32 v68, v47
	v_add_f32_e32 v50, v40, v85
	v_cvt_pk_f16_f32 v40, v80, v81
	v_cvt_pk_f16_f32 v41, v82, v83
	v_cvt_pk_f16_f32 v42, v84, v85
	v_cvt_pk_f16_f32 v43, v86, v87
	ds_read_b64_tr_b16 v[44:45], v187 offset:32768
	ds_read_b64_tr_b16 v[46:47], v187 offset:33280
	v_add_f32_e32 v50, v50, v86
	v_add_f32_e32 v54, v50, v87
	ds_read_b64_tr_b16 v[50:51], v187 offset:33792
	ds_read_b64_tr_b16 v[52:53], v187 offset:34304
	s_waitcnt lgkmcnt(2)
	v_mfma_f32_32x32x16_f16 v[0:15], v[40:43], v[44:47], v[0:15]
	ds_read_b64_tr_b16 v[44:45], v187 offset:36864
	ds_read_b64_tr_b16 v[46:47], v187 offset:37376
	v_add_f32_e32 v54, v54, v88
	v_add_f32_e32 v69, v54, v89
	v_cvt_pk_f16_f32 v54, v88, v89
	v_cvt_pk_f16_f32 v55, v90, v91
	v_cvt_pk_f16_f32 v56, v92, v93
	v_cvt_pk_f16_f32 v57, v94, v95
	s_waitcnt lgkmcnt(0)
	v_mfma_f32_32x32x16_f16 v[16:31], v[40:43], v[44:47], v[16:31]
	v_add_f32_e32 v40, v69, v90
	v_add_f32_e32 v40, v40, v91
	v_add_f32_e32 v40, v40, v92
	v_add_f32_e32 v40, v40, v93
	ds_read_b64_tr_b16 v[58:59], v187 offset:37888
	ds_read_b64_tr_b16 v[60:61], v187 offset:38400
	v_add_f32_e32 v40, v40, v94
	v_add_f32_e32 v40, v40, v95
	v_mfma_f32_32x32x16_f16 v[0:15], v[54:57], v[50:53], v[0:15]
	v_add_f32_e32 v40, v40, v32
	v_add_f32_e32 v50, v40, v33
	v_cvt_pk_f16_f32 v40, v32, v33
	v_cvt_pk_f16_f32 v41, v34, v35
	v_cvt_pk_f16_f32 v42, v36, v37
	v_cvt_pk_f16_f32 v43, v38, v39
	ds_read_b64_tr_b16 v[44:45], v187 offset:34816
	ds_read_b64_tr_b16 v[46:47], v187 offset:35328
	s_waitcnt lgkmcnt(2)
	v_mfma_f32_32x32x16_f16 v[16:31], v[54:57], v[58:61], v[16:31]
	v_add_f32_e32 v32, v50, v34
	v_add_f32_e32 v50, v32, v35
	ds_read_b64_tr_b16 v[32:33], v187 offset:35840
	ds_read_b64_tr_b16 v[34:35], v187 offset:36352
	v_add_f32_e32 v36, v50, v36
	v_add_f32_e32 v36, v36, v37
	v_cvt_pk_f16_f32 v50, v49, v62
	v_cvt_pk_f16_f32 v51, v63, v64
	s_waitcnt lgkmcnt(2)
	v_mfma_f32_32x32x16_f16 v[0:15], v[40:43], v[44:47], v[0:15]
	ds_read_b64_tr_b16 v[44:45], v187 offset:38912
	ds_read_b64_tr_b16 v[46:47], v187 offset:39424
	v_cvt_pk_f16_f32 v52, v65, v66
	v_cvt_pk_f16_f32 v53, v67, v68
	ds_read_b64_tr_b16 v[54:55], v187 offset:39936
	ds_read_b64_tr_b16 v[56:57], v187 offset:40448
	v_add_f32_e32 v36, v36, v38
	v_add_f32_e32 v36, v36, v39
	v_add_f32_e32 v36, v36, v49
	s_waitcnt lgkmcnt(2)
	v_mfma_f32_32x32x16_f16 v[16:31], v[40:43], v[44:47], v[16:31]
	v_add_f32_e32 v36, v36, v62
	v_mfma_f32_32x32x16_f16 v[0:15], v[50:53], v[32:35], v[0:15]
	v_add_f32_e32 v32, v36, v63
	v_add_f32_e32 v32, v32, v64
	v_add_f32_e32 v32, v32, v65
	v_add_f32_e32 v32, v32, v66
	v_add_f32_e32 v32, v32, v67
	v_add_f32_e32 v32, v32, v68
	v_add_f32_e32 v32, v188, v32
	s_waitcnt lgkmcnt(0)
	v_mfma_f32_32x32x16_f16 v[16:31], v[50:53], v[54:57], v[16:31]
	v_mov_b32_e32 v33, v32
	s_nop 1
	v_permlane32_swap_b32_e32 v32, v33
	s_and_saveexec_b64 s[2:3], s[0:1]
	v_add_f32_e32 v32, v32, v33
	ds_write_b32 v186, v32 offset:49280
	s_or_b64 exec, exec, s[2:3]
	s_waitcnt lgkmcnt(0)
	ds_read_b128 v[32:35], v48 offset:49280
	ds_read_b128 v[36:39], v48 offset:49312
	s_lshl_b64 s[0:1], s[10:11], 2
	s_add_u32 s0, s6, s0
	s_addc_u32 s1, s7, s1
	s_waitcnt lgkmcnt(1)
	v_rcp_f32_e32 v40, v32
	v_rcp_f32_e32 v41, v33
	s_lshl_b32 s2, s20, 13
	v_rcp_f32_e32 v42, v34
	v_rcp_f32_e32 v43, v35
	s_waitcnt lgkmcnt(0)
	v_rcp_f32_e32 v44, v36
	ds_read_b128 v[32:35], v48 offset:49344
	v_rcp_f32_e32 v45, v37
	v_rcp_f32_e32 v46, v38
	v_rcp_f32_e32 v47, v39
	ds_read_b128 v[36:39], v48 offset:49376
	s_add_i32 s2, s2, 0
	v_lshlrev_b32_e32 v48, 2, v181
	v_add3_u32 v48, s2, v182, v48
	v_mul_f32_e32 v0, v0, v40
	v_mul_f32_e32 v16, v16, v40
	v_add_u32_e32 v40, 0xc800, v48
	ds_write2_b32 v40, v0, v16 offset1:32
	v_mul_f32_e32 v0, v1, v41
	v_mul_f32_e32 v1, v17, v41
	ds_write2_b32 v40, v0, v1 offset0:64 offset1:96
	v_mul_f32_e32 v0, v2, v42
	v_mul_f32_e32 v1, v18, v42
	ds_write2_b32 v40, v0, v1 offset0:128 offset1:160
	v_mul_f32_e32 v0, v3, v43
	v_mul_f32_e32 v1, v19, v43
	s_waitcnt lgkmcnt(4)
	v_rcp_f32_e32 v32, v32
	ds_write2_b32 v40, v0, v1 offset0:192 offset1:224
	v_mul_f32_e32 v0, v4, v44
	v_mul_f32_e32 v1, v20, v44
	v_add_u32_e32 v2, 0xd000, v48
	v_rcp_f32_e32 v33, v33
	ds_write2_b32 v2, v0, v1 offset1:32
	v_mul_f32_e32 v0, v5, v45
	v_mul_f32_e32 v1, v21, v45
	v_rcp_f32_e32 v34, v34
	ds_write2_b32 v2, v0, v1 offset0:64 offset1:96
	v_mul_f32_e32 v0, v6, v46
	v_mul_f32_e32 v1, v22, v46
	v_rcp_f32_e32 v35, v35
	ds_write2_b32 v2, v0, v1 offset0:128 offset1:160
	v_mul_f32_e32 v0, v7, v47
	v_mul_f32_e32 v1, v23, v47
	s_waitcnt lgkmcnt(7)
	v_rcp_f32_e32 v36, v36
	ds_write2_b32 v2, v0, v1 offset0:192 offset1:224
	v_mul_f32_e32 v0, v8, v32
	v_mul_f32_e32 v1, v24, v32
	v_add_u32_e32 v2, 0xd800, v48
	v_rcp_f32_e32 v37, v37
	ds_write2_b32 v2, v0, v1 offset1:32
	v_mul_f32_e32 v0, v9, v33
	v_mul_f32_e32 v1, v25, v33
	v_rcp_f32_e32 v38, v38
	ds_write2_b32 v2, v0, v1 offset0:64 offset1:96
	v_mul_f32_e32 v0, v10, v34
	v_mul_f32_e32 v1, v26, v34
	v_rcp_f32_e32 v39, v39
	ds_write2_b32 v2, v0, v1 offset0:128 offset1:160
	v_mul_f32_e32 v0, v11, v35
	v_mul_f32_e32 v1, v27, v35
	ds_write2_b32 v2, v0, v1 offset0:192 offset1:224
	v_mul_f32_e32 v0, v12, v36
	v_mul_f32_e32 v1, v28, v36
	v_add_u32_e32 v2, 0xe000, v48
	ds_write2_b32 v2, v0, v1 offset1:32
	v_mul_f32_e32 v0, v13, v37
	v_mul_f32_e32 v1, v29, v37
	ds_write2_b32 v2, v0, v1 offset0:64 offset1:96
	v_mul_f32_e32 v0, v14, v38
	v_mul_f32_e32 v1, v30, v38
	ds_write2_b32 v2, v0, v1 offset0:128 offset1:160
	v_mul_f32_e32 v0, v15, v39
	v_mul_f32_e32 v1, v31, v39
	v_and_b32_e32 v8, 0xf0, v185
	ds_write2_b32 v2, v0, v1 offset0:192 offset1:224
	v_add_u32_e32 v14, s2, v8
	s_waitcnt lgkmcnt(0)
	v_lshl_add_u32 v0, v183, 8, v14
	v_or_b32_e32 v15, 4, v183
	s_lshl_b32 s3, s21, 2
	ds_read_b128 v[0:3], v0 offset:51200
	v_lshl_add_u32 v4, v15, 8, v14
	s_add_u32 s0, s0, s3
	ds_read_b128 v[4:7], v4 offset:51200
	s_addc_u32 s1, s1, 0
	v_mov_b32_e32 v9, 0
	v_lshl_add_u64 v[10:11], s[0:1], 0, v[8:9]
	v_lshlrev_b32_e32 v8, 11, v183
	v_lshl_add_u64 v[12:13], v[10:11], 0, v[8:9]
	v_lshlrev_b32_e32 v8, 11, v15
	s_waitcnt lgkmcnt(1)
	global_store_dwordx4 v[12:13], v[0:3], off sc1 nt
	v_or_b32_e32 v15, 12, v183
	s_nop 0
	v_lshl_add_u64 v[0:1], v[10:11], 0, v[8:9]
	s_waitcnt lgkmcnt(0)
	global_store_dwordx4 v[0:1], v[4:7], off sc1 nt
	s_nop 1
	v_or_b32_e32 v4, 8, v183
	v_lshl_add_u32 v0, v4, 8, v14
	ds_read_b128 v[0:3], v0 offset:51200
	v_lshlrev_b32_e32 v8, 11, v4
	v_lshl_add_u32 v4, v15, 8, v14
	ds_read_b128 v[4:7], v4 offset:51200
	v_lshl_add_u64 v[12:13], v[10:11], 0, v[8:9]
	v_lshlrev_b32_e32 v8, 11, v15
	s_waitcnt lgkmcnt(1)
	global_store_dwordx4 v[12:13], v[0:3], off sc1 nt
	v_or_b32_e32 v15, 20, v183
	s_nop 0
	v_lshl_add_u64 v[0:1], v[10:11], 0, v[8:9]
	s_waitcnt lgkmcnt(0)
	global_store_dwordx4 v[0:1], v[4:7], off sc1 nt
	s_nop 1
	v_or_b32_e32 v4, 16, v183
	v_lshl_add_u32 v0, v4, 8, v14
	ds_read_b128 v[0:3], v0 offset:51200
	v_lshlrev_b32_e32 v8, 11, v4
	v_lshl_add_u32 v4, v15, 8, v14
	ds_read_b128 v[4:7], v4 offset:51200
	v_lshl_add_u64 v[12:13], v[10:11], 0, v[8:9]
	v_lshlrev_b32_e32 v8, 11, v15
	s_waitcnt lgkmcnt(1)
	global_store_dwordx4 v[12:13], v[0:3], off sc1 nt
	v_or_b32_e32 v15, 28, v183
	s_nop 0
	v_lshl_add_u64 v[0:1], v[10:11], 0, v[8:9]
	s_waitcnt lgkmcnt(0)
	global_store_dwordx4 v[0:1], v[4:7], off sc1 nt
	s_nop 1
	v_or_b32_e32 v4, 24, v183
	v_lshl_add_u32 v0, v4, 8, v14
	ds_read_b128 v[0:3], v0 offset:51200
	v_lshlrev_b32_e32 v8, 11, v4
	v_lshl_add_u32 v4, v15, 8, v14
	ds_read_b128 v[4:7], v4 offset:51200
	v_lshl_add_u64 v[12:13], v[10:11], 0, v[8:9]
	v_lshlrev_b32_e32 v8, 11, v15
	s_waitcnt lgkmcnt(1)
	global_store_dwordx4 v[12:13], v[0:3], off sc1 nt
	s_nop 1
	v_lshl_add_u64 v[0:1], v[10:11], 0, v[8:9]
	s_waitcnt lgkmcnt(0)
	global_store_dwordx4 v[0:1], v[4:7], off sc1 nt
	s_endpgm
